# adds: P10 the 16 histogram loads of a row block issued with the block's first load batch (one round trip instead of two)
# baseline (speedup 1.0000x reference)
.LBB0_1153:
	s_lshl_b32 s40, s39, 5
	s_add_i32 s12, s40, s35
	s_ashr_i32 s13, s12, 31
	s_lshl_b64 s[24:25], s[12:13], 2
	s_add_u32 s24, s33, s24
	s_addc_u32 s25, s34, s25
	s_lshl_b64 s[26:27], s[12:13], 12
	v_lshl_add_u64 v[90:91], v[40:41], 0, s[26:27]
	global_load_dwordx2 v[150:151], v[90:91], off
	global_load_dwordx2 v[152:153], v[90:91], off offset:512
	global_load_dwordx2 v[154:155], v[90:91], off offset:1024
	global_load_dwordx4 v[2:5], v39, s[24:25]
	global_load_dwordx4 v[34:37], v[42:43], off
	global_load_dwordx4 v[30:33], v[42:43], off offset:1024
	global_load_dwordx4 v[26:29], v[42:43], off offset:2048
	global_load_dwordx4 v[22:25], v[42:43], off offset:3072
	global_load_dwordx4 v[18:21], v[44:45], off
	global_load_dwordx4 v[14:17], v[46:47], off
	global_load_dwordx4 v[10:13], v[48:49], off
	global_load_dwordx4 v[6:9], v[50:51], off
	global_load_dwordx2 v[156:157], v[90:91], off offset:1536
	global_load_dwordx2 v[158:159], v[90:91], off offset:2048
	global_load_dwordx2 v[160:161], v[90:91], off offset:2560
	global_load_dwordx2 v[162:163], v[90:91], off offset:3072
	global_load_dwordx2 v[164:165], v[90:91], off offset:3584
	s_or_b32 s28, s12, 1
	s_or_b32 s26, s12, 2
	s_or_b32 s24, s12, 3
	s_ashr_i32 s29, s28, 31
	s_ashr_i32 s27, s26, 31
	s_ashr_i32 s25, s24, 31
	s_lshl_b64 s[30:31], s[28:29], 12
	s_lshl_b64 s[42:43], s[26:27], 12
	s_lshl_b64 s[44:45], s[24:25], 12
	v_lshl_add_u64 v[90:91], v[40:41], 0, s[30:31]
	v_lshl_add_u64 v[92:93], v[40:41], 0, s[42:43]
	v_lshl_add_u64 v[166:167], v[40:41], 0, s[44:45]
	global_load_dwordx2 v[168:169], v[90:91], off
	global_load_dwordx2 v[170:171], v[90:91], off offset:512
	global_load_dwordx2 v[172:173], v[90:91], off offset:1024
	global_load_dwordx2 v[174:175], v[90:91], off offset:1536
	global_load_dwordx2 v[128:129], v[90:91], off offset:2048
	global_load_dwordx2 v[126:127], v[90:91], off offset:2560
	global_load_dwordx2 v[124:125], v[90:91], off offset:3072
	global_load_dwordx2 v[122:123], v[90:91], off offset:3584
	global_load_dwordx2 v[120:121], v[92:93], off
	global_load_dwordx2 v[118:119], v[92:93], off offset:512
	global_load_dwordx2 v[116:117], v[92:93], off offset:1024
	global_load_dwordx2 v[114:115], v[92:93], off offset:1536
	global_load_dwordx2 v[112:113], v[92:93], off offset:2048
	global_load_dwordx2 v[110:111], v[92:93], off offset:2560
	global_load_dwordx2 v[108:109], v[92:93], off offset:3072
	global_load_dwordx2 v[106:107], v[92:93], off offset:3584
	global_load_dwordx2 v[104:105], v[166:167], off
	global_load_dwordx2 v[102:103], v[166:167], off offset:512
	global_load_dwordx2 v[100:101], v[166:167], off offset:1024
	global_load_dwordx2 v[98:99], v[166:167], off offset:1536
	global_load_dwordx2 v[96:97], v[166:167], off offset:2048
	global_load_dwordx2 v[94:95], v[166:167], off offset:2560
	global_load_dwordx2 v[92:93], v[166:167], off offset:3072
	global_load_dwordx2 v[90:91], v[166:167], off offset:3584
	global_load_dword v198, v[54:55], off
	global_load_dword v199, v[56:57], off
	global_load_dword v200, v[58:59], off
	global_load_dword v201, v[60:61], off
	global_load_dword v202, v[62:63], off
	global_load_dword v203, v[64:65], off
	global_load_dword v204, v[66:67], off
	global_load_dword v205, v[68:69], off
	global_load_dword v206, v[70:71], off
	global_load_dword v207, v[72:73], off
	global_load_dword v208, v[74:75], off
	global_load_dword v209, v[76:77], off
	global_load_dword v210, v[78:79], off
	global_load_dword v211, v[80:81], off
	global_load_dword v212, v[82:83], off
	global_load_dword v213, v[84:85], off
	v_mov_b32_e32 v177, 0
	v_mov_b32_e32 v176, 0
	s_lshl_b64 s[12:13], s[12:13], 11
	s_waitcnt vmcnt(0)
	v_lshlrev_b32_e32 v166, 16, v150
	v_lshlrev_b32_e32 v178, 16, v152
	v_and_b32_e32 v152, 0xffff0000, v152
	v_mul_f32_e32 v178, v2, v178
	v_mul_f32_e32 v152, v2, v152
	v_mul_f32_e32 v178, v178, v30
	v_mul_f32_e32 v152, v152, v31
	v_and_b32_e32 v150, 0xffff0000, v150
	v_cvt_pk_fp8_f32 v177, v178, v152
	v_lshlrev_b32_e32 v179, 16, v153
	v_and_b32_e32 v153, 0xffff0000, v153
	v_mul_f32_e32 v166, v2, v166
	v_mul_f32_e32 v150, v2, v150
	v_mul_f32_e32 v179, v2, v179
	v_mul_f32_e32 v153, v2, v153
	v_mul_f32_e32 v166, v166, v34
	v_mul_f32_e32 v150, v150, v35
	v_lshlrev_b32_e32 v180, 16, v154
	v_and_b32_e32 v154, 0xffff0000, v154
	v_mul_f32_e32 v179, v179, v32
	v_cvt_pk_fp8_f32 v176, v166, v150
	v_mul_f32_e32 v150, v153, v33
	v_lshlrev_b32_e32 v167, 16, v151
	v_and_b32_e32 v151, 0xffff0000, v151
	v_mul_f32_e32 v180, v2, v180
	v_cvt_pk_fp8_f32 v177, v179, v150 op_sel:[0,0,1]
	v_mul_f32_e32 v150, v2, v154
	v_mul_f32_e32 v167, v2, v167
	v_mul_f32_e32 v151, v2, v151
	v_mul_f32_e32 v152, v180, v26
	v_mul_f32_e32 v150, v150, v27
	v_mov_b32_e32 v153, 0
	v_mul_f32_e32 v167, v167, v36
	v_mul_f32_e32 v151, v151, v37
	v_cvt_pk_fp8_f32 v153, v152, v150
	v_cvt_pk_fp8_f32 v176, v167, v151 op_sel:[0,0,1]
	v_lshlrev_b32_e32 v151, 16, v155
	v_and_b32_e32 v150, 0xffff0000, v155
	v_mul_f32_e32 v151, v2, v151
	v_mul_f32_e32 v150, v2, v150
	v_mul_f32_e32 v151, v151, v28
	v_mul_f32_e32 v150, v150, v29
	v_cvt_pk_fp8_f32 v153, v151, v150 op_sel:[0,0,1]
	v_lshlrev_b32_e32 v150, 16, v156
	v_and_b32_e32 v151, 0xffff0000, v156
	v_mul_f32_e32 v150, v2, v150
	v_mul_f32_e32 v151, v2, v151
	v_mul_f32_e32 v150, v150, v22
	v_mul_f32_e32 v151, v151, v23
	v_mov_b32_e32 v154, 0
	v_cvt_pk_fp8_f32 v154, v150, v151
	v_lshlrev_b32_e32 v152, 16, v157
	v_and_b32_e32 v150, 0xffff0000, v157
	v_mul_f32_e32 v152, v2, v152
	v_mul_f32_e32 v150, v2, v150
	v_mul_f32_e32 v152, v152, v24
	v_mul_f32_e32 v150, v150, v25
	v_cvt_pk_fp8_f32 v154, v152, v150 op_sel:[0,0,1]
	v_lshlrev_b32_e32 v150, 16, v158
	v_and_b32_e32 v151, 0xffff0000, v158
	v_mul_f32_e32 v150, v2, v150
	v_mul_f32_e32 v151, v2, v151
	v_mul_f32_e32 v150, v150, v18
	v_mul_f32_e32 v151, v151, v19
	v_mov_b32_e32 v155, 0
	v_cvt_pk_fp8_f32 v155, v150, v151
	v_lshlrev_b32_e32 v152, 16, v159
	v_and_b32_e32 v150, 0xffff0000, v159
	v_mul_f32_e32 v152, v2, v152
	v_mul_f32_e32 v150, v2, v150
	v_mul_f32_e32 v152, v152, v20
	v_mul_f32_e32 v150, v150, v21
	v_cvt_pk_fp8_f32 v155, v152, v150 op_sel:[0,0,1]
	v_lshlrev_b32_e32 v150, 16, v160
	v_and_b32_e32 v151, 0xffff0000, v160
	v_mul_f32_e32 v150, v2, v150
	v_mul_f32_e32 v151, v2, v151
	v_mul_f32_e32 v150, v150, v14
	v_mul_f32_e32 v151, v151, v15
	v_mov_b32_e32 v156, 0
	v_cvt_pk_fp8_f32 v156, v150, v151
	v_lshlrev_b32_e32 v152, 16, v161
	v_and_b32_e32 v150, 0xffff0000, v161
	v_mul_f32_e32 v152, v2, v152
	v_mul_f32_e32 v150, v2, v150
	v_mul_f32_e32 v152, v152, v16
	v_mul_f32_e32 v150, v150, v17
	v_cvt_pk_fp8_f32 v156, v152, v150 op_sel:[0,0,1]
	v_lshlrev_b32_e32 v150, 16, v162
	v_and_b32_e32 v151, 0xffff0000, v162
	v_mul_f32_e32 v150, v2, v150
	v_mul_f32_e32 v151, v2, v151
	v_mul_f32_e32 v150, v150, v10
	v_mul_f32_e32 v151, v151, v11
	v_mov_b32_e32 v157, 0
	v_cvt_pk_fp8_f32 v157, v150, v151
	v_lshlrev_b32_e32 v152, 16, v163
	v_and_b32_e32 v150, 0xffff0000, v163
	v_mul_f32_e32 v152, v2, v152
	v_mul_f32_e32 v150, v2, v150
	v_mul_f32_e32 v152, v152, v12
	v_mul_f32_e32 v150, v150, v13
	v_cvt_pk_fp8_f32 v157, v152, v150 op_sel:[0,0,1]
	v_lshlrev_b32_e32 v150, 16, v164
	v_and_b32_e32 v151, 0xffff0000, v164
	v_mul_f32_e32 v150, v2, v150
	v_mul_f32_e32 v151, v2, v151
	v_mul_f32_e32 v150, v150, v6
	v_mul_f32_e32 v151, v151, v7
	v_mov_b32_e32 v158, 0
	v_cvt_pk_fp8_f32 v158, v150, v151
	v_lshlrev_b32_e32 v152, 16, v165
	v_and_b32_e32 v150, 0xffff0000, v165
	v_mul_f32_e32 v152, v2, v152
	v_mul_f32_e32 v2, v2, v150
	v_mul_f32_e32 v152, v152, v8
	v_mul_f32_e32 v2, v2, v9
	v_cvt_pk_fp8_f32 v158, v152, v2 op_sel:[0,0,1]
	v_lshlrev_b32_e32 v2, 16, v168
	v_and_b32_e32 v150, 0xffff0000, v168
	v_mul_f32_e32 v2, v3, v2
	v_mul_f32_e32 v150, v3, v150
	v_mul_f32_e32 v2, v2, v34
	v_mul_f32_e32 v150, v150, v35
	v_mov_b32_e32 v152, 0
	v_cvt_pk_fp8_f32 v152, v2, v150
	v_lshlrev_b32_e32 v151, 16, v169
	v_and_b32_e32 v2, 0xffff0000, v169
	v_mul_f32_e32 v151, v3, v151
	v_mul_f32_e32 v2, v3, v2
	v_mul_f32_e32 v151, v151, v36
	v_mul_f32_e32 v2, v2, v37
	v_cvt_pk_fp8_f32 v152, v151, v2 op_sel:[0,0,1]
	v_lshlrev_b32_e32 v2, 16, v170
	v_and_b32_e32 v150, 0xffff0000, v170
	v_mul_f32_e32 v2, v3, v2
	v_mul_f32_e32 v150, v3, v150
	ds_write2st64_b32 v130, v176, v177 offset0:64 offset1:65
	ds_write2st64_b32 v130, v153, v154 offset0:66 offset1:67
	ds_write2st64_b32 v130, v155, v156 offset0:68 offset1:69
	ds_write2st64_b32 v130, v157, v158 offset0:70 offset1:71
	v_mul_f32_e32 v2, v2, v30
	v_mul_f32_e32 v150, v150, v31
	v_mov_b32_e32 v153, 0
	v_cvt_pk_fp8_f32 v153, v2, v150
	v_lshlrev_b32_e32 v151, 16, v171
	v_and_b32_e32 v2, 0xffff0000, v171
	v_mul_f32_e32 v151, v3, v151
	v_mul_f32_e32 v2, v3, v2
	v_mul_f32_e32 v151, v151, v32
	v_mul_f32_e32 v2, v2, v33
	v_cvt_pk_fp8_f32 v153, v151, v2 op_sel:[0,0,1]
	v_lshlrev_b32_e32 v2, 16, v172
	v_and_b32_e32 v150, 0xffff0000, v172
	v_mul_f32_e32 v2, v3, v2
	v_mul_f32_e32 v150, v3, v150
	v_mul_f32_e32 v2, v2, v26
	v_mul_f32_e32 v150, v150, v27
	v_mov_b32_e32 v154, 0
	v_cvt_pk_fp8_f32 v154, v2, v150
	v_lshlrev_b32_e32 v151, 16, v173
	v_and_b32_e32 v2, 0xffff0000, v173
	v_mul_f32_e32 v151, v3, v151
	v_mul_f32_e32 v2, v3, v2
	v_mul_f32_e32 v151, v151, v28
	v_mul_f32_e32 v2, v2, v29
	v_cvt_pk_fp8_f32 v154, v151, v2 op_sel:[0,0,1]
	v_lshlrev_b32_e32 v2, 16, v174
	v_and_b32_e32 v150, 0xffff0000, v174
	v_mul_f32_e32 v2, v3, v2
	v_mul_f32_e32 v150, v3, v150
	v_mul_f32_e32 v2, v2, v22
	v_mul_f32_e32 v150, v150, v23
	v_mov_b32_e32 v155, 0
	v_cvt_pk_fp8_f32 v155, v2, v150
	v_lshlrev_b32_e32 v151, 16, v175
	v_and_b32_e32 v2, 0xffff0000, v175
	v_mul_f32_e32 v151, v3, v151
	v_mul_f32_e32 v2, v3, v2
	v_mul_f32_e32 v151, v151, v24
	v_mul_f32_e32 v2, v2, v25
	v_cvt_pk_fp8_f32 v155, v151, v2 op_sel:[0,0,1]
	v_lshlrev_b32_e32 v2, 16, v128
	v_and_b32_e32 v128, 0xffff0000, v128
	v_mul_f32_e32 v2, v3, v2
	v_mul_f32_e32 v128, v3, v128
	v_mul_f32_e32 v2, v2, v18
	v_mul_f32_e32 v128, v128, v19
	v_mov_b32_e32 v151, 0
	v_cvt_pk_fp8_f32 v151, v2, v128
	v_lshlrev_b32_e32 v150, 16, v129
	v_and_b32_e32 v2, 0xffff0000, v129
	v_mul_f32_e32 v150, v3, v150
	v_mul_f32_e32 v2, v3, v2
	v_mul_f32_e32 v150, v150, v20
	v_mul_f32_e32 v2, v2, v21
	v_cvt_pk_fp8_f32 v151, v150, v2 op_sel:[0,0,1]
	v_lshlrev_b32_e32 v2, 16, v126
	v_and_b32_e32 v126, 0xffff0000, v126
	v_mul_f32_e32 v2, v3, v2
	v_mul_f32_e32 v126, v3, v126
	v_mul_f32_e32 v2, v2, v14
	v_mul_f32_e32 v126, v126, v15
	v_mov_b32_e32 v129, 0
	v_cvt_pk_fp8_f32 v129, v2, v126
	v_lshlrev_b32_e32 v128, 16, v127
	v_and_b32_e32 v2, 0xffff0000, v127
	v_mul_f32_e32 v128, v3, v128
	v_mul_f32_e32 v2, v3, v2
	v_mul_f32_e32 v128, v128, v16
	v_mul_f32_e32 v2, v2, v17
	v_cvt_pk_fp8_f32 v129, v128, v2 op_sel:[0,0,1]
	v_lshlrev_b32_e32 v2, 16, v124
	v_and_b32_e32 v124, 0xffff0000, v124
	v_mul_f32_e32 v2, v3, v2
	v_mul_f32_e32 v124, v3, v124
	v_mul_f32_e32 v2, v2, v10
	v_mul_f32_e32 v124, v124, v11
	v_mov_b32_e32 v127, 0
	v_cvt_pk_fp8_f32 v127, v2, v124
	v_lshlrev_b32_e32 v126, 16, v125
	v_and_b32_e32 v2, 0xffff0000, v125
	v_mul_f32_e32 v126, v3, v126
	v_mul_f32_e32 v2, v3, v2
	v_mul_f32_e32 v126, v126, v12
	v_mul_f32_e32 v2, v2, v13
	v_cvt_pk_fp8_f32 v127, v126, v2 op_sel:[0,0,1]
	v_lshlrev_b32_e32 v2, 16, v122
	v_and_b32_e32 v122, 0xffff0000, v122
	v_mul_f32_e32 v2, v3, v2
	v_mul_f32_e32 v122, v3, v122
	v_mul_f32_e32 v2, v2, v6
	v_mul_f32_e32 v122, v122, v7
	v_mov_b32_e32 v125, 0
	v_cvt_pk_fp8_f32 v125, v2, v122
	v_lshlrev_b32_e32 v124, 16, v123
	v_and_b32_e32 v2, 0xffff0000, v123
	v_mul_f32_e32 v124, v3, v124
	v_mul_f32_e32 v2, v3, v2
	v_mul_f32_e32 v124, v124, v8
	v_mul_f32_e32 v2, v2, v9
	v_cvt_pk_fp8_f32 v125, v124, v2 op_sel:[0,0,1]
	v_lshlrev_b32_e32 v2, 16, v120
	v_and_b32_e32 v3, 0xffff0000, v120
	v_mul_f32_e32 v2, v4, v2
	v_mul_f32_e32 v3, v4, v3
	v_mul_f32_e32 v2, v2, v34
	v_mul_f32_e32 v3, v3, v35
	v_mov_b32_e32 v122, 0
	v_cvt_pk_fp8_f32 v122, v2, v3
	v_lshlrev_b32_e32 v120, 16, v121
	v_and_b32_e32 v2, 0xffff0000, v121
	v_mul_f32_e32 v120, v4, v120
	v_mul_f32_e32 v2, v4, v2
	v_mul_f32_e32 v120, v120, v36
	v_mul_f32_e32 v2, v2, v37
	v_cvt_pk_fp8_f32 v122, v120, v2 op_sel:[0,0,1]
	v_lshlrev_b32_e32 v2, 16, v118
	v_and_b32_e32 v3, 0xffff0000, v118
	v_mul_f32_e32 v2, v4, v2
	v_mul_f32_e32 v3, v4, v3
	v_mul_f32_e32 v2, v2, v30
	v_mul_f32_e32 v3, v3, v31
	v_mov_b32_e32 v120, 0
	v_cvt_pk_fp8_f32 v120, v2, v3
	v_lshlrev_b32_e32 v118, 16, v119
	v_and_b32_e32 v2, 0xffff0000, v119
	v_mul_f32_e32 v118, v4, v118
	v_mul_f32_e32 v2, v4, v2
	v_mul_f32_e32 v118, v118, v32
	v_mul_f32_e32 v2, v2, v33
	v_cvt_pk_fp8_f32 v120, v118, v2 op_sel:[0,0,1]
	v_lshlrev_b32_e32 v2, 16, v116
	v_and_b32_e32 v3, 0xffff0000, v116
	v_mul_f32_e32 v2, v4, v2
	v_mul_f32_e32 v3, v4, v3
	v_mul_f32_e32 v2, v2, v26
	v_mul_f32_e32 v3, v3, v27
	v_mov_b32_e32 v118, 0
	v_cvt_pk_fp8_f32 v118, v2, v3
	v_lshlrev_b32_e32 v116, 16, v117
	v_and_b32_e32 v2, 0xffff0000, v117
	v_mul_f32_e32 v116, v4, v116
	v_mul_f32_e32 v2, v4, v2
	v_mul_f32_e32 v116, v116, v28
	v_mul_f32_e32 v2, v2, v29
	v_cvt_pk_fp8_f32 v118, v116, v2 op_sel:[0,0,1]
	v_lshlrev_b32_e32 v2, 16, v114
	v_and_b32_e32 v3, 0xffff0000, v114
	v_mul_f32_e32 v2, v4, v2
	v_mul_f32_e32 v3, v4, v3
	v_mul_f32_e32 v2, v2, v22
	v_mul_f32_e32 v3, v3, v23
	v_mov_b32_e32 v116, 0
	v_cvt_pk_fp8_f32 v116, v2, v3
	v_lshlrev_b32_e32 v114, 16, v115
	v_and_b32_e32 v2, 0xffff0000, v115
	v_mul_f32_e32 v114, v4, v114
	v_mul_f32_e32 v2, v4, v2
	v_mul_f32_e32 v114, v114, v24
	v_mul_f32_e32 v2, v2, v25
	v_cvt_pk_fp8_f32 v116, v114, v2 op_sel:[0,0,1]
	v_lshlrev_b32_e32 v2, 16, v112
	v_and_b32_e32 v3, 0xffff0000, v112
	v_mul_f32_e32 v2, v4, v2
	v_mul_f32_e32 v3, v4, v3
	v_mul_f32_e32 v2, v2, v18
	v_mul_f32_e32 v3, v3, v19
	v_mov_b32_e32 v114, 0
	v_cvt_pk_fp8_f32 v114, v2, v3
	v_lshlrev_b32_e32 v112, 16, v113
	v_and_b32_e32 v2, 0xffff0000, v113
	v_mul_f32_e32 v112, v4, v112
	v_mul_f32_e32 v2, v4, v2
	v_mul_f32_e32 v112, v112, v20
	v_mul_f32_e32 v2, v2, v21
	v_cvt_pk_fp8_f32 v114, v112, v2 op_sel:[0,0,1]
	v_lshlrev_b32_e32 v2, 16, v110
	v_and_b32_e32 v3, 0xffff0000, v110
	v_mul_f32_e32 v2, v4, v2
	v_mul_f32_e32 v3, v4, v3
	v_mul_f32_e32 v2, v2, v14
	v_mul_f32_e32 v3, v3, v15
	v_mov_b32_e32 v112, 0
	v_cvt_pk_fp8_f32 v112, v2, v3
	v_lshlrev_b32_e32 v110, 16, v111
	v_and_b32_e32 v2, 0xffff0000, v111
	v_mul_f32_e32 v110, v4, v110
	v_mul_f32_e32 v2, v4, v2
	v_mul_f32_e32 v110, v110, v16
	v_mul_f32_e32 v2, v2, v17
	v_cvt_pk_fp8_f32 v112, v110, v2 op_sel:[0,0,1]
	v_lshlrev_b32_e32 v2, 16, v108
	v_and_b32_e32 v3, 0xffff0000, v108
	v_mul_f32_e32 v2, v4, v2
	v_mul_f32_e32 v3, v4, v3
	v_mul_f32_e32 v2, v2, v10
	v_mul_f32_e32 v3, v3, v11
	v_mov_b32_e32 v110, 0
	v_cvt_pk_fp8_f32 v110, v2, v3
	v_lshlrev_b32_e32 v108, 16, v109
	v_and_b32_e32 v2, 0xffff0000, v109
	v_mul_f32_e32 v108, v4, v108
	v_mul_f32_e32 v2, v4, v2
	v_mul_f32_e32 v108, v108, v12
	v_mul_f32_e32 v2, v2, v13
	v_cvt_pk_fp8_f32 v110, v108, v2 op_sel:[0,0,1]
	v_lshlrev_b32_e32 v2, 16, v106
	v_and_b32_e32 v3, 0xffff0000, v106
	v_mul_f32_e32 v2, v4, v2
	v_mul_f32_e32 v3, v4, v3
	v_mul_f32_e32 v2, v2, v6
	v_mul_f32_e32 v3, v3, v7
	v_mov_b32_e32 v108, 0
	v_cvt_pk_fp8_f32 v108, v2, v3
	v_lshlrev_b32_e32 v106, 16, v107
	v_and_b32_e32 v2, 0xffff0000, v107
	v_mul_f32_e32 v106, v4, v106
	v_mul_f32_e32 v2, v4, v2
	v_mul_f32_e32 v106, v106, v8
	v_mul_f32_e32 v2, v2, v9
	v_cvt_pk_fp8_f32 v108, v106, v2 op_sel:[0,0,1]
	v_lshlrev_b32_e32 v2, 16, v104
	v_and_b32_e32 v3, 0xffff0000, v104
	v_mul_f32_e32 v2, v5, v2
	v_mul_f32_e32 v3, v5, v3
	v_mul_f32_e32 v2, v2, v34
	v_mul_f32_e32 v3, v3, v35
	v_mov_b32_e32 v34, 0
	v_cvt_pk_fp8_f32 v34, v2, v3
	v_lshlrev_b32_e32 v4, 16, v105
	v_and_b32_e32 v2, 0xffff0000, v105
	v_mul_f32_e32 v4, v5, v4
	v_mul_f32_e32 v2, v5, v2
	v_mul_f32_e32 v4, v4, v36
	v_mul_f32_e32 v2, v2, v37
	v_cvt_pk_fp8_f32 v34, v4, v2 op_sel:[0,0,1]
	v_lshlrev_b32_e32 v2, 16, v102
	v_and_b32_e32 v3, 0xffff0000, v102
	v_mul_f32_e32 v2, v5, v2
	v_mul_f32_e32 v3, v5, v3
	v_mul_f32_e32 v2, v2, v30
	v_mul_f32_e32 v3, v3, v31
	v_mov_b32_e32 v30, 0
	v_cvt_pk_fp8_f32 v30, v2, v3
	v_lshlrev_b32_e32 v4, 16, v103
	v_and_b32_e32 v2, 0xffff0000, v103
	v_mul_f32_e32 v4, v5, v4
	v_mul_f32_e32 v2, v5, v2
	v_mul_f32_e32 v4, v4, v32
	v_mul_f32_e32 v2, v2, v33
	v_cvt_pk_fp8_f32 v30, v4, v2 op_sel:[0,0,1]
	v_lshlrev_b32_e32 v2, 16, v100
	v_and_b32_e32 v3, 0xffff0000, v100
	v_mul_f32_e32 v2, v5, v2
	v_mul_f32_e32 v3, v5, v3
	v_mul_f32_e32 v2, v2, v26
	v_mul_f32_e32 v3, v3, v27
	v_mov_b32_e32 v26, 0
	v_cvt_pk_fp8_f32 v26, v2, v3
	v_lshlrev_b32_e32 v4, 16, v101
	v_and_b32_e32 v2, 0xffff0000, v101
	v_mul_f32_e32 v4, v5, v4
	v_mul_f32_e32 v2, v5, v2
	v_mul_f32_e32 v4, v4, v28
	v_mul_f32_e32 v2, v2, v29
	v_cvt_pk_fp8_f32 v26, v4, v2 op_sel:[0,0,1]
	v_lshlrev_b32_e32 v2, 16, v98
	v_and_b32_e32 v3, 0xffff0000, v98
	v_mul_f32_e32 v2, v5, v2
	v_mul_f32_e32 v3, v5, v3
	v_mul_f32_e32 v2, v2, v22
	v_mul_f32_e32 v3, v3, v23
	v_mov_b32_e32 v22, 0
	v_cvt_pk_fp8_f32 v22, v2, v3
	v_lshlrev_b32_e32 v4, 16, v99
	v_and_b32_e32 v2, 0xffff0000, v99
	v_mul_f32_e32 v4, v5, v4
	v_mul_f32_e32 v2, v5, v2
	v_mul_f32_e32 v4, v4, v24
	v_mul_f32_e32 v2, v2, v25
	v_cvt_pk_fp8_f32 v22, v4, v2 op_sel:[0,0,1]
	v_lshlrev_b32_e32 v2, 16, v96
	v_and_b32_e32 v3, 0xffff0000, v96
	v_mul_f32_e32 v2, v5, v2
	v_mul_f32_e32 v3, v5, v3
	v_mul_f32_e32 v2, v2, v18
	v_mul_f32_e32 v3, v3, v19
	v_mov_b32_e32 v18, 0
	v_cvt_pk_fp8_f32 v18, v2, v3
	v_lshlrev_b32_e32 v4, 16, v97
	v_and_b32_e32 v2, 0xffff0000, v97
	v_mul_f32_e32 v4, v5, v4
	v_mul_f32_e32 v2, v5, v2
	v_mul_f32_e32 v4, v4, v20
	v_mul_f32_e32 v2, v2, v21
	v_cvt_pk_fp8_f32 v18, v4, v2 op_sel:[0,0,1]
	v_lshlrev_b32_e32 v2, 16, v94
	v_and_b32_e32 v3, 0xffff0000, v94
	v_mul_f32_e32 v2, v5, v2
	v_mul_f32_e32 v3, v5, v3
	v_mul_f32_e32 v2, v2, v14
	v_mul_f32_e32 v3, v3, v15
	v_mov_b32_e32 v14, 0
	v_cvt_pk_fp8_f32 v14, v2, v3
	v_lshlrev_b32_e32 v4, 16, v95
	v_and_b32_e32 v2, 0xffff0000, v95
	v_mul_f32_e32 v4, v5, v4
	v_mul_f32_e32 v2, v5, v2
	v_mul_f32_e32 v4, v4, v16
	v_mul_f32_e32 v2, v2, v17
	v_cvt_pk_fp8_f32 v14, v4, v2 op_sel:[0,0,1]
	v_lshlrev_b32_e32 v2, 16, v92
	v_and_b32_e32 v3, 0xffff0000, v92
	v_mul_f32_e32 v2, v5, v2
	v_mul_f32_e32 v3, v5, v3
	v_mul_f32_e32 v2, v2, v10
	v_mul_f32_e32 v3, v3, v11
	v_mov_b32_e32 v10, 0
	v_cvt_pk_fp8_f32 v10, v2, v3
	v_lshlrev_b32_e32 v4, 16, v93
	v_and_b32_e32 v2, 0xffff0000, v93
	v_mul_f32_e32 v4, v5, v4
	v_mul_f32_e32 v2, v5, v2
	v_mul_f32_e32 v4, v4, v12
	v_mul_f32_e32 v2, v2, v13
	v_cvt_pk_fp8_f32 v10, v4, v2 op_sel:[0,0,1]
	v_lshlrev_b32_e32 v2, 16, v90
	v_and_b32_e32 v3, 0xffff0000, v90
	v_mul_f32_e32 v2, v5, v2
	v_mul_f32_e32 v3, v5, v3
	v_mul_f32_e32 v2, v2, v6
	v_mul_f32_e32 v3, v3, v7
	v_mov_b32_e32 v6, 0
	v_cvt_pk_fp8_f32 v6, v2, v3
	v_lshlrev_b32_e32 v4, 16, v91
	v_and_b32_e32 v2, 0xffff0000, v91
	v_mul_f32_e32 v4, v5, v4
	v_mul_f32_e32 v2, v5, v2
	v_mul_f32_e32 v4, v4, v8
	v_mul_f32_e32 v2, v2, v9
	v_cvt_pk_fp8_f32 v6, v4, v2 op_sel:[0,0,1]
	ds_write2st64_b32 v130, v152, v153 offset0:72 offset1:73
	ds_write2st64_b32 v130, v154, v155 offset0:74 offset1:75
	ds_write2st64_b32 v130, v151, v129 offset0:76 offset1:77
	ds_write2st64_b32 v130, v127, v125 offset0:78 offset1:79
	ds_write2st64_b32 v130, v122, v120 offset0:80 offset1:81
	ds_write2st64_b32 v130, v118, v116 offset0:82 offset1:83
	ds_write2st64_b32 v130, v114, v112 offset0:84 offset1:85
	ds_write2st64_b32 v130, v110, v108 offset0:86 offset1:87
	ds_write2st64_b32 v130, v34, v30 offset0:88 offset1:89
	ds_write2st64_b32 v130, v26, v22 offset0:90 offset1:91
	ds_write2st64_b32 v130, v18, v14 offset0:92 offset1:93
	ds_write2st64_b32 v130, v10, v6 offset0:94 offset1:95
	s_waitcnt lgkmcnt(0)
	v_add_u32_e32 v12, s38, v38
	ds_read_b128 v[2:5], v12 offset:16384
	ds_read_b128 v[6:9], v12 offset:17408
	v_lshl_add_u64 v[10:11], v[52:53], 0, s[12:13]
	s_lshl_b64 s[12:13], s[28:29], 11
	s_waitcnt lgkmcnt(1)
	global_store_dwordx4 v[10:11], v[2:5], off
	ds_read_b128 v[2:5], v12 offset:18432
	s_waitcnt lgkmcnt(1)
	global_store_dwordx4 v[10:11], v[6:9], off offset:1024
	v_lshl_add_u64 v[10:11], v[52:53], 0, s[12:13]
	ds_read_b128 v[6:9], v12 offset:19456
	s_lshl_b64 s[12:13], s[26:27], 11
	s_waitcnt lgkmcnt(1)
	global_store_dwordx4 v[10:11], v[2:5], off
	ds_read_b128 v[2:5], v12 offset:20480
	v_lshl_add_u64 v[14:15], v[52:53], 0, s[12:13]
	s_waitcnt lgkmcnt(1)
	global_store_dwordx4 v[10:11], v[6:9], off offset:1024
	ds_read_b128 v[6:9], v12 offset:21504
	s_lshl_b64 s[12:13], s[24:25], 11
	s_waitcnt lgkmcnt(1)
	global_store_dwordx4 v[14:15], v[2:5], off
	ds_read_b128 v[2:5], v12 offset:22528
	ds_read_b128 v[10:13], v12 offset:23552
	s_waitcnt lgkmcnt(2)
	global_store_dwordx4 v[14:15], v[6:9], off offset:1024
	s_nop 1
	v_lshl_add_u64 v[6:7], v[52:53], 0, s[12:13]
	s_waitcnt lgkmcnt(1)
	global_store_dwordx4 v[6:7], v[2:5], off
	s_waitcnt lgkmcnt(0)
	global_store_dwordx4 v[6:7], v[10:13], off offset:1024
	v_cmp_gt_i32_e64 s[12:13], s39, v131
	s_nop 0
	s_nop 0
	v_cndmask_b32_e64 v18, 0, v198, s[12:13]
	v_cmp_gt_i32_e64 s[12:13], s39, v132
	s_nop 0
	v_add_u32_e32 v2, v199, v198
	s_nop 0
	v_add3_u32 v2, v2, v200, v201
	v_cndmask_b32_e64 v3, 0, v199, s[12:13]
	v_cmp_gt_i32_e64 s[12:13], s39, v133
	v_add_u32_e32 v3, v3, v18
	s_nop 0
	v_add3_u32 v2, v2, v202, v203
	v_cndmask_b32_e64 v18, 0, v200, s[12:13]
	v_cmp_gt_i32_e64 s[12:13], s39, v134
	s_nop 0
	v_add3_u32 v2, v2, v204, v205
	s_nop 0
	v_add3_u32 v2, v2, v206, v207
	v_cndmask_b32_e64 v4, 0, v201, s[12:13]
	v_cmp_gt_i32_e64 s[12:13], s39, v135
	v_add3_u32 v3, v3, v18, v4
	s_nop 0
	v_add3_u32 v2, v2, v208, v209
	v_cndmask_b32_e64 v4, 0, v202, s[12:13]
	v_cmp_gt_i32_e64 s[12:13], s39, v136
	s_nop 0
	v_add3_u32 v2, v2, v210, v211
	s_nop 0
	v_add3_u32 v2, v2, v212, v213
	v_cndmask_b32_e64 v5, 0, v203, s[12:13]
	v_cmp_gt_i32_e64 s[12:13], s39, v137
	v_add3_u32 v3, v3, v4, v5
	s_nop 0
	v_cndmask_b32_e64 v4, 0, v204, s[12:13]
	v_cmp_gt_i32_e64 s[12:13], s39, v138
	s_nop 1
	v_cndmask_b32_e64 v5, 0, v205, s[12:13]
	v_cmp_gt_i32_e64 s[12:13], s39, v139
	v_add3_u32 v3, v3, v4, v5
	s_nop 0
	v_cndmask_b32_e64 v4, 0, v206, s[12:13]
	v_cmp_gt_i32_e64 s[12:13], s39, v140
	s_nop 1
	v_cndmask_b32_e64 v5, 0, v207, s[12:13]
	v_cmp_gt_i32_e64 s[12:13], s39, v141
	v_add3_u32 v3, v3, v4, v5
	s_nop 0
	v_cndmask_b32_e64 v4, 0, v208, s[12:13]
	v_cmp_gt_i32_e64 s[12:13], s39, v142
	s_nop 1
	v_cndmask_b32_e64 v5, 0, v209, s[12:13]
	v_cmp_gt_i32_e64 s[12:13], s39, v143
	v_add3_u32 v3, v3, v4, v5
	s_nop 0
	v_cndmask_b32_e64 v4, 0, v210, s[12:13]
	v_cmp_gt_i32_e64 s[12:13], s39, v144
	s_nop 1
	v_cndmask_b32_e64 v5, 0, v211, s[12:13]
	v_cmp_gt_i32_e64 s[12:13], s39, v145
	v_add3_u32 v3, v3, v4, v5
	s_nop 0
	v_cndmask_b32_e64 v4, 0, v212, s[12:13]
	v_cmp_gt_i32_e64 s[12:13], s39, v146
	s_nop 1
	v_cndmask_b32_e64 v5, 0, v213, s[12:13]
	v_add3_u32 v3, v3, v4, v5
	ds_write2st64_b32 v147, v2, v3 offset1:8
	v_lshl_or_b32 v2, s39, 7, v0
	s_and_saveexec_b64 s[12:13], vcc
	s_cbranch_execz .LBB0_1155
	v_ashrrev_i32_e32 v3, 31, v2
	v_lshl_add_u64 v[4:5], v[2:3], 2, s[14:15]
	global_load_dword v3, v[4:5], off
	s_waitcnt vmcnt(0)
	ds_write_b32 v147, v3 offset:4224
